# dense attention loop: the nine scalar bumps that sat in front of the loop-closing barrier moved behind it (pole waves reach the barrier sooner)
# baseline (speedup 1.0000x reference)
; #define WAIT_BAR(N) asm volatile("s_waitcnt vmcnt(" #N ") lgkmcnt(0)\n\ts_barrier":::"memory")
;   #define ROT() do{sl_prev=sl_cur;sl_cur=sl_next;sl_next=sl_nx2;sl_nx2=(sl_nx2==(NSLOT-1)*SLOTB)?0:sl_nx2+SLOTB;}while(0)
; template<int THRL> __device__ __forceinline__ void attn_unit(int b,int qb,const unsigned char*Q,const unsigned char*__restrict__ K,const unsigned char*__restrict__ VT,unsigned char*O,char*shm){
;     ...
;     for(;t+5<NT;t+=2){
;       STEP(p8B,p8A,t,true,true,true);     WAIT_BAR(4); ROT();
;       STEP(p8A,p8B,t+1,true,true,true);   WAIT_BAR(4); ROT();
;     }
.LBB0_333:
	v_add_u32_e32 v16, s19, v155
	s_waitcnt lgkmcnt(1)
	v_mfma_scale_f32_32x32x64_f8f6f4 v[82:97], v[122:129], v[106:113], v[50:65], v164, v163 op_sel_hi:[0,0,0]
	ds_read_b128 v[122:125], v16 offset:16384
	ds_read_b128 v[166:169], v16 offset:16896
	ds_read_b128 v[126:129], v16 offset:17408
	ds_read_b128 v[170:173], v16 offset:17920
	s_waitcnt lgkmcnt(4)
	v_mfma_scale_f32_32x32x64_f8f6f4 v[66:81], v[130:137], v[106:113], v[50:65], v164, v163 op_sel_hi:[0,0,0]
	s_add_u32 s76, s56, 0x8000
	s_addc_u32 s77, s57, 0
	s_add_i32 s19, vcc_hi, s0
	s_mov_b32 s91, m0
	s_mov_b32 m0, s19
	s_mov_b32 exec_hi, 0
	global_load_lds_dwordx4 v153, s[76:77]
	s_mov_b32 exec_hi, -1
	s_mov_b32 m0, s91
	s_add_i32 s19, vcc_lo, s1
	s_mov_b32 s76, m0
	s_mov_b32 m0, s19
	s_mov_b32 exec_hi, 0
	global_load_lds_dwordx4 v154, s[58:59]
	s_mov_b32 exec_hi, -1
	s_mov_b32 m0, s76
	v_add_u32_e32 v16, s90, v155
	s_waitcnt lgkmcnt(1)
	v_mfma_scale_f32_32x32x64_f8f6f4 v[34:49], v[4:11], v[122:129], v[34:49], v164, v164 op_sel_hi:[0,0,0] cbsz:1
	ds_read_b128 v[122:125], v16
	ds_read_b128 v[126:129], v16 offset:1024
	s_nop 4
	v_cvt_pknorm_u16_f32 v17, v82, v83
	v_cvt_pknorm_u16_f32 v82, v84, v85
	v_cvt_pknorm_u16_f32 v83, v86, v87
	v_cvt_pknorm_u16_f32 v84, v88, v89
	v_cvt_pknorm_u16_f32 v85, v90, v91
	v_cvt_pknorm_u16_f32 v86, v92, v93
	v_cvt_pknorm_u16_f32 v87, v94, v95
	v_cvt_pknorm_u16_f32 v88, v96, v97
	v_perm_b32 v114, v82, v17, s82
	v_perm_b32 v115, v84, v83, s82
	v_perm_b32 v116, v86, v85, s82
	v_perm_b32 v117, v88, v87, s82
	v_or3_b32 v3, v3, v114, v115
	s_nop 0
	v_or3_b32 v3, v3, v116, v117
	ds_read_b128 v[130:133], v16 offset:512
	ds_read_b128 v[134:137], v16 offset:1536
	v_cvt_pknorm_u16_f32 v16, v66, v67
	v_cvt_pknorm_u16_f32 v17, v68, v69
	v_cvt_pknorm_u16_f32 v66, v70, v71
	v_cvt_pknorm_u16_f32 v67, v72, v73
	v_cvt_pknorm_u16_f32 v68, v74, v75
	v_cvt_pknorm_u16_f32 v69, v76, v77
	v_cvt_pknorm_u16_f32 v70, v78, v79
	v_cvt_pknorm_u16_f32 v71, v80, v81
	s_waitcnt lgkmcnt(4)
	v_mfma_scale_f32_32x32x64_f8f6f4 v[18:33], v[4:11], v[166:173], v[18:33], v164, v164 op_sel_hi:[0,0,0] cbsz:1
	v_perm_b32 v118, v17, v16, s82
	v_perm_b32 v119, v67, v66, s82
	v_perm_b32 v120, v69, v68, s82
	v_perm_b32 v121, v71, v70, s82
	v_or3_b32 v3, v3, v118, v119
	s_nop 0
	v_or3_b32 v3, v3, v120, v121
	v_mfma_scale_f32_16x16x128_f8f6f4 v[12:15], v[4:11], v[98:105], v[12:15], v164, v164 op_sel_hi:[0,0,0] cbsz:1
	s_waitcnt vmcnt(4) lgkmcnt(0)
	s_barrier
	s_add_i32 s19, vcc_lo, 0x1000
	s_cmpk_lg_i32 vcc_lo, 0x3000
	s_cselect_b32 s91, s19, 0
	v_add_u32_e32 v4, vcc_hi, v155
	s_waitcnt lgkmcnt(2)
	v_mfma_scale_f32_32x32x64_f8f6f4 v[82:97], v[122:129], v[106:113], v[50:65], v164, v163 op_sel_hi:[0,0,0]
	ds_read_b128 v[122:125], v4 offset:16384
	ds_read_b128 v[166:169], v4 offset:16896
	ds_read_b128 v[126:129], v4 offset:17408
	ds_read_b128 v[170:173], v4 offset:17920
	s_waitcnt lgkmcnt(4)
	v_mfma_scale_f32_32x32x64_f8f6f4 v[66:81], v[130:137], v[106:113], v[50:65], v164, v163 op_sel_hi:[0,0,0]
	s_add_u32 s76, s56, 0xa000
	s_addc_u32 s77, s57, 0
	s_add_i32 s19, s90, s0
	s_mov_b32 vcc_hi, m0
	s_mov_b32 m0, s19
	s_mov_b32 exec_hi, 0
	global_load_lds_dwordx4 v153, s[76:77]
	s_mov_b32 exec_hi, -1
	s_mov_b32 m0, vcc_hi
	s_add_u32 s76, s60, 0xc0
	s_addc_u32 s77, s61, 0
	s_add_i32 s19, s91, s1
	s_mov_b32 vcc_hi, m0
	s_mov_b32 m0, s19
	s_mov_b32 exec_hi, 0
	global_load_lds_dwordx4 v154, s[76:77]
	s_mov_b32 exec_hi, -1
	s_mov_b32 m0, vcc_hi
	v_add_u32_e32 v16, vcc_lo, v155
	s_waitcnt lgkmcnt(1)
	v_mfma_scale_f32_32x32x64_f8f6f4 v[34:49], v[114:121], v[122:129], v[34:49], v164, v164 op_sel_hi:[0,0,0] cbsz:1
	ds_read_b128 v[122:125], v16
	ds_read_b128 v[126:129], v16 offset:1024
	s_nop 2
	v_cvt_pknorm_u16_f32 v4, v82, v83
	v_cvt_pknorm_u16_f32 v5, v84, v85
	v_cvt_pknorm_u16_f32 v6, v86, v87
	v_cvt_pknorm_u16_f32 v7, v88, v89
	v_cvt_pknorm_u16_f32 v17, v90, v91
	v_cvt_pknorm_u16_f32 v82, v92, v93
	v_cvt_pknorm_u16_f32 v83, v94, v95
	v_cvt_pknorm_u16_f32 v84, v96, v97
	v_perm_b32 v4, v5, v4, s82
	v_perm_b32 v5, v7, v6, s82
	v_perm_b32 v6, v82, v17, s82
	v_perm_b32 v7, v84, v83, s82
	v_or3_b32 v3, v3, v4, v5
	s_nop 0
	v_or3_b32 v3, v3, v6, v7
	ds_read_b128 v[130:133], v16 offset:512
	ds_read_b128 v[134:137], v16 offset:1536
	v_cvt_pknorm_u16_f32 v8, v66, v67
	v_cvt_pknorm_u16_f32 v9, v68, v69
	v_cvt_pknorm_u16_f32 v10, v70, v71
	v_cvt_pknorm_u16_f32 v11, v72, v73
	v_cvt_pknorm_u16_f32 v16, v74, v75
	v_cvt_pknorm_u16_f32 v17, v76, v77
	v_cvt_pknorm_u16_f32 v66, v78, v79
	v_cvt_pknorm_u16_f32 v67, v80, v81
	s_waitcnt lgkmcnt(4)
	v_mfma_scale_f32_32x32x64_f8f6f4 v[18:33], v[114:121], v[166:173], v[18:33], v164, v164 op_sel_hi:[0,0,0] cbsz:1
	v_perm_b32 v8, v9, v8, s82
	v_perm_b32 v9, v11, v10, s82
	v_perm_b32 v10, v17, v16, s82
	v_perm_b32 v11, v67, v66, s82
	v_or3_b32 v3, v3, v8, v9
	s_nop 0
	v_or3_b32 v3, v3, v10, v11
	v_mfma_scale_f32_16x16x128_f8f6f4 v[12:15], v[114:121], v[98:105], v[12:15], v164, v164 op_sel_hi:[0,0,0] cbsz:1
	s_waitcnt vmcnt(4) lgkmcnt(0)
	s_barrier
	s_add_i32 s76, s91, 0x1000
	s_cmpk_lg_i32 s91, 0x3000
	s_mov_b32 vcc_hi, vcc_lo
	s_cselect_b32 vcc_lo, s76, 0
	s_add_i32 s33, s33, 2
	s_add_u32 s60, s60, 0x80
	s_addc_u32 s61, s61, 0
	s_add_u32 s58, s58, 0x80
	s_addc_u32 s59, s59, 0
	s_add_u32 s56, s56, 0x4000
	s_addc_u32 s57, s57, 0
	s_mov_b32 s19, s90
	s_mov_b32 s90, s91
	s_cmpk_gt_u32 s33, 0x78
	s_cbranch_scc0 .LBB0_333
;   #define ROT() do{sl_prev=sl_cur;sl_cur=sl_next;sl_next=sl_nx2;sl_nx2=(sl_nx2==(NSLOT-1)*SLOTB)?0:sl_nx2+SLOTB;}while(0)
;   #define ENDW(tt) do{ if((tt)+4<NT){WAIT_BAR(4);} else if((tt)+3<NT){WAIT_BAR(3);} else if((tt)+2<NT){WAIT_BAR(2);} else {WAIT_BAR(0);} }while(0)
; template<int THRL> __device__ __forceinline__ void attn_unit(int b,int qb,const unsigned char*Q,const unsigned char*__restrict__ K,const unsigned char*__restrict__ VT,unsigned char*O,char*shm){
;     ...
;     for(;t+1<NT;t+=2){
;       STEP(p8B,p8A,t,(t+4<NT),(t+2<NT),(t+1<NT));       ENDW(t);   ROT();
;       STEP(p8A,p8B,t+1,(t+5<NT),(t+3<NT),(t+2<NT));     ENDW(t+1); ROT();
;     }
	s_waitcnt lgkmcnt(2)
	v_mfma_scale_f32_32x32x64_f8f6f4 v[82:97], v[122:129], v[106:113], v[50:65], v164, v163 op_sel_hi:[0,0,0]
	ds_read_b128 v[122:125], v155 offset:24576
	ds_read_b128 v[166:169], v155 offset:25088
	ds_read_b128 v[126:129], v155 offset:25600
	ds_read_b128 v[170:173], v155 offset:26112
	s_waitcnt lgkmcnt(4)
	v_mfma_scale_f32_32x32x64_f8f6f4 v[66:81], v[130:137], v[106:113], v[50:65], v164, v163 op_sel_hi:[0,0,0]
	s_cmp_lg_u32 0, -1
	s_cselect_b32 s19, 0, 0
	s_add_i32 s19, s19, s14
	s_add_i32 s33, s19, 0x3000
	s_mov_b32 s56, m0
	s_mov_b32 m0, s33
	s_mov_b32 exec_hi, 0
	global_load_lds_dwordx4 v153, s[40:41]
	s_mov_b32 exec_hi, -1
	s_mov_b32 m0, s56
	s_add_i32 s33, s19, 0x5000
	s_mov_b32 s56, m0
	s_mov_b32 m0, s33
	s_mov_b32 exec_hi, 0
	global_load_lds_dwordx4 v154, s[42:43]
	s_mov_b32 exec_hi, -1
	s_mov_b32 m0, s56
	s_waitcnt lgkmcnt(1)
	v_mfma_scale_f32_32x32x64_f8f6f4 v[34:49], v[4:11], v[122:129], v[34:49], v164, v164 op_sel_hi:[0,0,0] cbsz:1
	ds_read_b128 v[122:125], v155
	ds_read_b128 v[126:129], v155 offset:1024
	s_nop 4
	v_cvt_pknorm_u16_f32 v16, v82, v83
	v_cvt_pknorm_u16_f32 v17, v84, v85
	v_cvt_pknorm_u16_f32 v82, v86, v87
	v_cvt_pknorm_u16_f32 v83, v88, v89
	v_cvt_pknorm_u16_f32 v84, v90, v91
	v_cvt_pknorm_u16_f32 v85, v92, v93
	v_cvt_pknorm_u16_f32 v86, v94, v95
	v_cvt_pknorm_u16_f32 v87, v96, v97
	v_perm_b32 v114, v17, v16, s82
	v_perm_b32 v115, v83, v82, s82
	v_perm_b32 v116, v85, v84, s82
	v_perm_b32 v117, v87, v86, s82
	v_or3_b32 v3, v3, v114, v115
	s_nop 0
	v_or3_b32 v3, v3, v116, v117
	ds_read_b128 v[130:133], v155 offset:512
	ds_read_b128 v[134:137], v155 offset:1536
	v_cvt_pknorm_u16_f32 v16, v66, v67
	v_cvt_pknorm_u16_f32 v17, v68, v69
	v_cvt_pknorm_u16_f32 v66, v70, v71
	v_cvt_pknorm_u16_f32 v67, v72, v73
	v_cvt_pknorm_u16_f32 v68, v74, v75
	v_cvt_pknorm_u16_f32 v69, v76, v77
	v_cvt_pknorm_u16_f32 v70, v78, v79
	v_cvt_pknorm_u16_f32 v71, v80, v81
	s_waitcnt lgkmcnt(4)
	v_mfma_scale_f32_32x32x64_f8f6f4 v[18:33], v[4:11], v[166:173], v[18:33], v164, v164 op_sel_hi:[0,0,0] cbsz:1
	v_perm_b32 v118, v17, v16, s82
	v_perm_b32 v119, v67, v66, s82
	v_perm_b32 v120, v69, v68, s82
	v_perm_b32 v121, v71, v70, s82
	v_or3_b32 v3, v3, v118, v119
	s_nop 0
	v_or3_b32 v3, v3, v120, v121
	v_mfma_scale_f32_16x16x128_f8f6f4 v[12:15], v[4:11], v[98:105], v[12:15], v164, v164 op_sel_hi:[0,0,0] cbsz:1
	s_waitcnt vmcnt(4) lgkmcnt(0)
	s_barrier
	s_waitcnt lgkmcnt(2)
	v_mfma_scale_f32_32x32x64_f8f6f4 v[82:97], v[122:129], v[106:113], v[50:65], v164, v163 op_sel_hi:[0,0,0]
	ds_read_b128 v[122:125], v155 offset:28672
	ds_read_b128 v[166:169], v155 offset:29184
	ds_read_b128 v[126:129], v155 offset:29696
	ds_read_b128 v[170:173], v155 offset:30208
	s_waitcnt lgkmcnt(4)
	v_mfma_scale_f32_32x32x64_f8f6f4 v[66:81], v[130:137], v[106:113], v[50:65], v164, v163 op_sel_hi:[0,0,0]
	s_add_i32 s33, s19, 0x6000
	s_mov_b32 s56, m0
	s_mov_b32 m0, s33
	s_mov_b32 exec_hi, 0
	global_load_lds_dwordx4 v154, s[44:45]
	s_mov_b32 exec_hi, -1
	s_mov_b32 m0, s56
	s_waitcnt lgkmcnt(1)
	v_mfma_scale_f32_32x32x64_f8f6f4 v[34:49], v[114:121], v[122:129], v[34:49], v164, v164 op_sel_hi:[0,0,0] cbsz:1
	ds_read_b128 v[122:125], v155 offset:4096
	ds_read_b128 v[126:129], v155 offset:5120
	s_nop 8
	v_cvt_pknorm_u16_f32 v4, v82, v83
	v_cvt_pknorm_u16_f32 v5, v84, v85
	v_cvt_pknorm_u16_f32 v6, v86, v87
	v_cvt_pknorm_u16_f32 v7, v88, v89
	v_cvt_pknorm_u16_f32 v16, v90, v91
	v_cvt_pknorm_u16_f32 v17, v92, v93
	v_cvt_pknorm_u16_f32 v82, v94, v95
	v_cvt_pknorm_u16_f32 v83, v96, v97
	v_perm_b32 v4, v5, v4, s82
	v_perm_b32 v5, v7, v6, s82
	v_perm_b32 v6, v17, v16, s82
	v_perm_b32 v7, v83, v82, s82
	v_or3_b32 v3, v3, v4, v5
	s_nop 0
	v_or3_b32 v3, v3, v6, v7
	ds_read_b128 v[130:133], v155 offset:4608
	ds_read_b128 v[134:137], v155 offset:5632
	v_cvt_pknorm_u16_f32 v8, v66, v67
	v_cvt_pknorm_u16_f32 v9, v68, v69
	v_cvt_pknorm_u16_f32 v10, v70, v71
	v_cvt_pknorm_u16_f32 v11, v72, v73
	v_cvt_pknorm_u16_f32 v16, v74, v75
	v_cvt_pknorm_u16_f32 v17, v76, v77
	v_cvt_pknorm_u16_f32 v66, v78, v79
	v_cvt_pknorm_u16_f32 v67, v80, v81
	s_waitcnt lgkmcnt(4)
	v_mfma_scale_f32_32x32x64_f8f6f4 v[18:33], v[114:121], v[166:173], v[18:33], v164, v164 op_sel_hi:[0,0,0] cbsz:1
	v_perm_b32 v8, v9, v8, s82
	v_perm_b32 v9, v11, v10, s82
	v_perm_b32 v10, v17, v16, s82
	v_perm_b32 v11, v67, v66, s82
	v_or3_b32 v3, v3, v8, v9
	s_nop 0
	v_or3_b32 v3, v3, v10, v11
	v_mfma_scale_f32_16x16x128_f8f6f4 v[12:15], v[114:121], v[98:105], v[12:15], v164, v164 op_sel_hi:[0,0,0] cbsz:1
	s_waitcnt vmcnt(3) lgkmcnt(0)
	s_barrier
; #define SBAR() __builtin_amdgcn_sched_barrier(0)
;   #define VRD(i) do{ vf[i]=*(const __attribute__((address_space(3))) bf16x8*)(vp_+((i)>>1)*512+((i)&1)*1024); }while(0)
;   #define ROT() do{sl_prev=sl_cur;sl_cur=sl_next;sl_next=sl_nx2;sl_nx2=(sl_nx2==(NSLOT-1)*SLOTB)?0:sl_nx2+SLOTB;}while(0)
;   #define ENDW(tt) do{ if((tt)+4<NT){WAIT_BAR(4);} else if((tt)+3<NT){WAIT_BAR(3);} else if((tt)+2<NT){WAIT_BAR(2);} else {WAIT_BAR(0);} }while(0)
; template<int THRL> __device__ __forceinline__ void attn_unit(int b,int qb,const unsigned char*Q,const unsigned char*__restrict__ K,const unsigned char*__restrict__ VT,unsigned char*O,char*shm){
;     ...
;     for(;t+1<NT;t+=2){
;       STEP(p8B,p8A,t,(t+4<NT),(t+2<NT),(t+1<NT));       ENDW(t);   ROT();
;       STEP(p8A,p8B,t+1,(t+5<NT),(t+3<NT),(t+2<NT));     ENDW(t+1); ROT();
;     }
;     STEP(p8B,p8A,NT-1,false,false,false);
;     { const lds_cptr vp_=vp0+sl_cur; VRD(0); VRD(1); VRD(2); VRD(3); SBAR();
;       o[0]=pv8(p8B,vf[0],vf[1],o[0]); o[1]=pv8(p8B,vf[2],vf[3],o[1]); o2=__builtin_amdgcn_mfma_scale_f32_16x16x128_f8f6f4(p8B,vones,o2,1,0,0,0x7f7f7f7f,0,0x7f7f7f7f); }
;     bool bad=__any((orv&0xC0C0C0C0u)!=0u);
;     ...
;     bad=true;
;     ...
;     if(lane==0)vflag[wid]=(bad&&attempt==0)?1u:0u;
	s_waitcnt lgkmcnt(2)
	v_mfma_scale_f32_32x32x64_f8f6f4 v[82:97], v[122:129], v[106:113], v[50:65], v164, v163 op_sel_hi:[0,0,0]
	ds_read_b128 v[122:125], v155 offset:16384
	ds_read_b128 v[166:169], v155 offset:16896
	ds_read_b128 v[126:129], v155 offset:17408
	ds_read_b128 v[170:173], v155 offset:17920
	s_waitcnt lgkmcnt(4)
	v_mfma_scale_f32_32x32x64_f8f6f4 v[66:81], v[130:137], v[106:113], v[50:65], v164, v163 op_sel_hi:[0,0,0]
	s_addk_i32 s19, 0x7000
	s_mov_b32 s33, m0
	s_mov_b32 m0, s19
	s_mov_b32 exec_hi, 0
	global_load_lds_dwordx4 v154, s[46:47]
	s_mov_b32 exec_hi, -1
	s_mov_b32 m0, s33
	s_waitcnt lgkmcnt(1)
	v_mfma_scale_f32_32x32x64_f8f6f4 v[34:49], v[4:11], v[122:129], v[34:49], v164, v164 op_sel_hi:[0,0,0] cbsz:1
	ds_read_b128 v[122:125], v155 offset:8192
	ds_read_b128 v[126:129], v155 offset:9216
	s_nop 8
	v_cvt_pknorm_u16_f32 v16, v82, v83
	v_cvt_pknorm_u16_f32 v17, v84, v85
	v_cvt_pknorm_u16_f32 v82, v86, v87
	v_cvt_pknorm_u16_f32 v83, v88, v89
	v_cvt_pknorm_u16_f32 v84, v90, v91
	v_cvt_pknorm_u16_f32 v85, v92, v93
	v_cvt_pknorm_u16_f32 v86, v94, v95
	v_cvt_pknorm_u16_f32 v87, v96, v97
	v_perm_b32 v114, v17, v16, s82
	v_perm_b32 v115, v83, v82, s82
	v_perm_b32 v116, v85, v84, s82
	v_perm_b32 v117, v87, v86, s82
	v_or3_b32 v3, v3, v114, v115
	s_nop 0
	v_or3_b32 v3, v3, v116, v117
	ds_read_b128 v[130:133], v155 offset:8704
	ds_read_b128 v[134:137], v155 offset:9728
	v_cvt_pknorm_u16_f32 v16, v66, v67
	v_cvt_pknorm_u16_f32 v17, v68, v69
	v_cvt_pknorm_u16_f32 v66, v70, v71
	v_cvt_pknorm_u16_f32 v67, v72, v73
	v_cvt_pknorm_u16_f32 v68, v74, v75
	v_cvt_pknorm_u16_f32 v69, v76, v77
	v_cvt_pknorm_u16_f32 v70, v78, v79
	v_cvt_pknorm_u16_f32 v71, v80, v81
	s_waitcnt lgkmcnt(4)
	v_mfma_scale_f32_32x32x64_f8f6f4 v[18:33], v[4:11], v[166:173], v[18:33], v164, v164 op_sel_hi:[0,0,0] cbsz:1
	v_perm_b32 v118, v17, v16, s82
	v_perm_b32 v119, v67, v66, s82
	v_perm_b32 v120, v69, v68, s82
	v_perm_b32 v121, v71, v70, s82
	v_or3_b32 v3, v3, v118, v119
	s_nop 0
	v_or3_b32 v3, v3, v120, v121
	v_mfma_scale_f32_16x16x128_f8f6f4 v[12:15], v[4:11], v[98:105], v[12:15], v164, v164 op_sel_hi:[0,0,0] cbsz:1
	s_waitcnt vmcnt(2) lgkmcnt(0)
	s_barrier
	s_waitcnt lgkmcnt(2)
	v_mfma_scale_f32_32x32x64_f8f6f4 v[82:97], v[122:129], v[106:113], v[50:65], v164, v163 op_sel_hi:[0,0,0]
	ds_read_b128 v[122:125], v155 offset:20480
	ds_read_b128 v[166:169], v155 offset:20992
	ds_read_b128 v[126:129], v155 offset:21504
	ds_read_b128 v[170:173], v155 offset:22016
	s_waitcnt lgkmcnt(4)
	v_mfma_scale_f32_32x32x64_f8f6f4 v[66:81], v[130:137], v[106:113], v[50:65], v164, v163 op_sel_hi:[0,0,0]
	s_waitcnt lgkmcnt(1)
	v_mfma_scale_f32_32x32x64_f8f6f4 v[34:49], v[114:121], v[122:129], v[34:49], v164, v164 op_sel_hi:[0,0,0] cbsz:1
	ds_read_b128 v[122:125], v155 offset:12288
	ds_read_b128 v[126:129], v155 offset:13312
	s_nop 9
	v_cvt_pknorm_u16_f32 v4, v82, v83
	v_cvt_pknorm_u16_f32 v5, v84, v85
	v_cvt_pknorm_u16_f32 v6, v86, v87
	v_cvt_pknorm_u16_f32 v7, v88, v89
	v_cvt_pknorm_u16_f32 v16, v90, v91
	v_cvt_pknorm_u16_f32 v17, v92, v93
	v_cvt_pknorm_u16_f32 v82, v94, v95
	v_cvt_pknorm_u16_f32 v83, v96, v97
	v_perm_b32 v4, v5, v4, s82
	v_perm_b32 v5, v7, v6, s82
	v_perm_b32 v6, v17, v16, s82
	v_perm_b32 v7, v83, v82, s82
	v_or3_b32 v3, v3, v4, v5
	s_nop 0
	v_or3_b32 v3, v3, v6, v7
	ds_read_b128 v[82:85], v155 offset:12800
	ds_read_b128 v[86:89], v155 offset:13824
	v_cvt_pknorm_u16_f32 v8, v66, v67
	v_cvt_pknorm_u16_f32 v9, v68, v69
	v_cvt_pknorm_u16_f32 v10, v70, v71
	v_cvt_pknorm_u16_f32 v11, v72, v73
	v_cvt_pknorm_u16_f32 v16, v74, v75
	v_cvt_pknorm_u16_f32 v17, v76, v77
	v_cvt_pknorm_u16_f32 v66, v78, v79
	v_cvt_pknorm_u16_f32 v67, v80, v81
	s_waitcnt lgkmcnt(4)
	v_mfma_scale_f32_32x32x64_f8f6f4 v[18:33], v[114:121], v[166:173], v[18:33], v164, v164 op_sel_hi:[0,0,0] cbsz:1
	v_perm_b32 v8, v9, v8, s82
	v_perm_b32 v9, v11, v10, s82
	v_perm_b32 v10, v17, v16, s82
	v_perm_b32 v11, v67, v66, s82
	v_or3_b32 v3, v3, v8, v9
	s_nop 0
	v_or3_b32 v3, v3, v10, v11
	v_mfma_scale_f32_16x16x128_f8f6f4 v[12:15], v[114:121], v[98:105], v[12:15], v164, v164 op_sel_hi:[0,0,0] cbsz:1
	s_waitcnt vmcnt(0) lgkmcnt(0)
	s_barrier
	s_waitcnt lgkmcnt(2)
	v_mfma_scale_f32_32x32x64_f8f6f4 v[66:81], v[122:129], v[106:113], v[50:65], v164, v163 op_sel_hi:[0,0,0]
	ds_read_b128 v[90:93], v155 offset:24576
	ds_read_b128 v[122:125], v155 offset:25088
	ds_read_b128 v[94:97], v155 offset:25600
	ds_read_b128 v[126:129], v155 offset:26112
	s_waitcnt lgkmcnt(4)
	v_mfma_scale_f32_32x32x64_f8f6f4 v[50:65], v[82:89], v[106:113], v[50:65], v164, v163 op_sel_hi:[0,0,0]
	s_nop 13
	v_cvt_pknorm_u16_f32 v16, v66, v67
	v_cvt_pknorm_u16_f32 v17, v68, v69
	v_cvt_pknorm_u16_f32 v66, v70, v71
	v_cvt_pknorm_u16_f32 v67, v72, v73
	v_cvt_pknorm_u16_f32 v68, v74, v75
	v_cvt_pknorm_u16_f32 v69, v76, v77
	v_cvt_pknorm_u16_f32 v70, v78, v79
	v_cvt_pknorm_u16_f32 v71, v80, v81
	s_waitcnt lgkmcnt(1)
	v_mfma_scale_f32_32x32x64_f8f6f4 v[34:49], v[4:11], v[90:97], v[34:49], v164, v164 op_sel_hi:[0,0,0] cbsz:1
	v_perm_b32 v114, v17, v16, s82
	v_perm_b32 v115, v67, v66, s82
	v_perm_b32 v116, v69, v68, s82
	v_perm_b32 v117, v71, v70, s82
	v_or3_b32 v3, v3, v114, v115
	s_nop 0
	v_or3_b32 v3, v3, v116, v117
	v_cvt_pknorm_u16_f32 v16, v50, v51
	v_cvt_pknorm_u16_f32 v17, v52, v53
	v_cvt_pknorm_u16_f32 v50, v54, v55
	v_cvt_pknorm_u16_f32 v51, v56, v57
	v_cvt_pknorm_u16_f32 v52, v58, v59
	v_cvt_pknorm_u16_f32 v53, v60, v61
	v_cvt_pknorm_u16_f32 v54, v62, v63
	v_cvt_pknorm_u16_f32 v55, v64, v65
	s_waitcnt lgkmcnt(0)
	v_mfma_scale_f32_32x32x64_f8f6f4 v[18:33], v[4:11], v[122:129], v[18:33], v164, v164 op_sel_hi:[0,0,0] cbsz:1
	v_perm_b32 v118, v17, v16, s82
	v_perm_b32 v119, v51, v50, s82
	v_perm_b32 v120, v53, v52, s82
	v_perm_b32 v121, v55, v54, s82
	v_or3_b32 v3, v3, v118, v119
	s_nop 0
	v_or3_b32 v3, v3, v120, v121
	v_mfma_scale_f32_16x16x128_f8f6f4 v[138:141], v[4:11], v[98:105], v[12:15], v164, v164 op_sel_hi:[0,0,0] cbsz:1
	ds_read_b128 v[122:125], v155 offset:28672
	ds_read_b128 v[130:133], v155 offset:29184
	ds_read_b128 v[126:129], v155 offset:29696
	ds_read_b128 v[134:137], v155 offset:30208
	v_and_b32_e32 v3, 0xc0c0c0c0, v3
	v_cmp_ne_u32_e32 vcc, 0, v3
	s_and_saveexec_b64 s[56:57], s[2:3]
	s_cbranch_execz .LBB0_336
	s_cmp_lg_u64 vcc, 0
	s_cselect_b64 s[58:59], -1, 0
	s_and_b64 s[54:55], s[54:55], s[58:59]
	v_cndmask_b32_e64 v3, 0, 1, s[54:55]
	v_mov_b32_e32 v4, s18
	ds_write_b32 v4, v3
